# v71 + the 24-state MFMA->VALU pad dropped in the four fp8 epilogues where >=28 independent instructions already precede the first accumulator read
# baseline (speedup 1.0000x reference)
;     __device__ __forceinline__ void operator()(AccRef acc, const GUnit& u, int wr, int wc, int fr, int fq) const {
;         const int pm = u.x0, pn = u.x1; const int col = pn * 256 + wc * 64 + 16 * fq;
; #pragma unroll
;         for (int ai = 0; ai < 2; ++ai)
; #pragma unroll
;             for (int m = 0; m < 4; ++m) { const int row = pm * 256 + ai * 128 + wr * 64 + m * 16 + fr; bf16* dst;
;                 if (pn < 4) dst = UF + (size_t)row * FW + col;
;                 else { const int g = (col - FW) >> 4, b = row >> 13, t = row & (SEQ - 1); dst = A2 + ((size_t)((g * 4 + b) * NCH + NCTXCH + (t >> 5)) * A2LD + (t & 31) * 16); }
;                 constexpr float SC = S8 ? W8_INV : 1.0f; st16_bf16(dst, acc[ai][0][m][0] * SC, acc[ai][0][m][1] * SC, acc[ai][1][m][0] * SC, acc[ai][1][m][1] * SC); }
.LBB0_375:
	s_lshl_b32 s19, s4, 8
	v_lshl_or_b32 v2, s66, 8, v206
	s_add_i32 s19, s19, s51
	s_cmp_gt_i32 s66, 3
	v_add_u32_e32 v3, 0xfffffc00, v2
	s_cselect_b64 s[26:27], -1, 0
	v_ashrrev_i32_e32 v10, 2, v3
	s_ashr_i32 s4, s19, 13
	v_add_u32_e32 v3, s4, v10
	v_mad_u64_u32 v[4:5], s[4:5], v3, s64, 8
	s_mov_b64 s[4:5], -1
	s_and_b64 vcc, exec, s[26:27]
	s_cbranch_vccz .LBB0_377
	s_lshr_b32 s4, s19, 5
	s_and_b32 s4, s4, 0xfe
	v_add_u32_e32 v3, s4, v4
	v_mad_i64_i32 v[6:7], s[4:5], v3, s65, v[182:183]
	s_mov_b64 s[4:5], 0

; __device__ __forceinline__ f32x4 u8x4_f32(unsigned w) { return (f32x4){(float)(w & 0xffu), (float)((w >> 8) & 0xffu), (float)((w >> 16) & 0xffu), (float)(w >> 24)}; }
; __device__ __forceinline__ unsigned pk4_fp8(float a, float b, float c, float d) { int w = 0; w = __builtin_amdgcn_cvt_pk_fp8_f32(clamp8(a), clamp8(b), w, false); w = __builtin_amdgcn_cvt_pk_fp8_f32(clamp8(c), clamp8(d), w, true); return (unsigned)w; }
; __host__ __device__ __forceinline__ size_t tiled_off(size_t r, int kb, int ktiles) { return (((r >> 8) * ktiles + (kb >> 7)) << 15) + ((r & 255) << 7) + (kb & 127); }
;     __device__ __forceinline__ void operator()(f32x4 (&acc)[2][2][4][2], const GUnit& u, int wr, int wc, int fr, int fq) const {
;     ...
; #pragma unroll
;         for (int ai = 0; ai < 2; ++ai) {
;             u32x4 qf[4];
; #pragma unroll
;             for (int m = 0; m < 4; ++m) qf[m] = __builtin_nontemporal_load((const u32x4*)(GZF + off0 + (size_t)(ai * 128 + m * 16) * D));
; #pragma unroll
;             for (int m = 0; m < 4; ++m) { u32x4 w;
; #pragma unroll
;                 for (int q = 0; q < 4; ++q) { const f32x4 f = u8x4_f32(qf[m][q]); const f32x4 a = acc[ai][q >> 1][m][q & 1]; f32x4 v;
; #pragma unroll
;                     for (int j = 0; j < 4; ++j) v[j] = a[j] * (fmaxf(f[j], 0.5f) * (W8_INV / 255.0f));
;                     w[q] = pk4_fp8(v[0], v[1], v[2], v[3]); }
;                 *(u32x4*)(M8 + tiled_off((size_t)(u.x0 * 256 + wr * 64 + fr + ai * 128 + m * 16), u.x1 * 256 + wc * 64 + 16 * fq, D / 128)) = w; }
;             asm volatile("" ::: "memory");
;         }
.LBB0_837:
	s_lshl_b32 s28, s71, 8
	v_add_u32_e32 v144, s28, v177
	v_ashrrev_i32_e32 v145, 31, v144
	s_lshl_b32 s26, s70, 8
	v_lshlrev_b64 v[2:3], 11, v[144:145]
	s_ashr_i32 s27, s26, 31
	v_lshl_add_u64 v[142:143], v[2:3], 0, s[26:27]
	v_or_b32_e32 v142, v142, v176
	s_cmp_lg_u32 s73, 0
	s_cselect_b64 s[24:25], -1, 0
	s_cmp_eq_u32 s73, 0
	v_lshl_add_u64 v[12:13], s[6:7], 0, v[142:143]
	s_cbranch_scc1 .LBB0_845
	global_load_dwordx4 v[146:149], v[12:13], off nt
	v_add_co_u32_e32 v2, vcc, 0x8000, v12
	v_mov_b32_e32 v151, 0
	s_nop 0
	v_addc_co_u32_e32 v3, vcc, 0, v13, vcc
	v_add_co_u32_e32 v4, vcc, 0x10000, v12
	v_mov_b32_e32 v150, 0
	s_nop 0
	v_addc_co_u32_e32 v5, vcc, 0, v13, vcc
	global_load_dwordx4 v[154:157], v[2:3], off nt
	global_load_dwordx4 v[6:9], v[4:5], off nt
	v_add_co_u32_e32 v188, vcc, 0x18000, v12
	v_mov_b32_e32 v152, 0
	s_nop 0
	v_addc_co_u32_e32 v189, vcc, 0, v13, vcc
	global_load_dwordx4 v[2:5], v[188:189], off nt
	s_or_b32 s26, s26, s53
	s_ashr_i32 s26, s26, 7
	s_ashr_i32 s27, s26, 31
	s_waitcnt vmcnt(0) lgkmcnt(0)
	v_cvt_f32_ubyte0_e32 v189, v147
	v_cvt_f32_ubyte1_e32 v201, v147
	v_max_f32_e32 v189, 0.5, v189
	v_max_f32_e32 v201, 0.5, v201
	v_mul_f32_e32 v189, 0x38808081, v189
	v_mul_f32_e32 v201, 0x38808081, v201
	v_cvt_f32_ubyte0_e32 v10, v146
	v_cvt_f32_ubyte1_e32 v153, v146
	v_cvt_f32_ubyte0_e32 v203, v148
	v_cvt_f32_ubyte1_e32 v204, v148
	v_mul_f32_e32 v189, v134, v189
	v_mul_f32_e32 v201, v135, v201
	v_cvt_f32_ubyte2_e32 v202, v147
	v_cvt_f32_ubyte3_e32 v147, v147
	v_max_f32_e32 v10, 0.5, v10
	v_max_f32_e32 v153, 0.5, v153
	v_max_f32_e32 v203, 0.5, v203
	v_max_f32_e32 v204, 0.5, v204
	v_med3_f32 v189, v189, s60, v200
	v_med3_f32 v201, v201, s60, v200
	v_cvt_f32_ubyte2_e32 v205, v148
	v_cvt_f32_ubyte3_e32 v148, v148
	v_max_f32_e32 v202, 0.5, v202
	v_max_f32_e32 v147, 0.5, v147
	v_mul_f32_e32 v10, 0x38808081, v10
	v_mul_f32_e32 v153, 0x38808081, v153
	v_mul_f32_e32 v203, 0x38808081, v203
	v_mul_f32_e32 v204, 0x38808081, v204
	v_cvt_pk_fp8_f32 v151, v189, v201
	v_max_f32_e32 v148, 0.5, v148
	v_mul_f32_e32 v202, 0x38808081, v202
	v_mul_f32_e32 v147, 0x38808081, v147
	v_mul_f32_e32 v10, v138, v10
	v_mul_f32_e32 v153, v139, v153
	v_mul_f32_e32 v203, v106, v203
	v_mul_f32_e32 v204, v107, v204
	v_cvt_f32_ubyte2_e32 v188, v146
	v_cvt_f32_ubyte3_e32 v146, v146
	v_mul_f32_e32 v148, 0x38808081, v148
	v_mul_f32_e32 v202, v136, v202
	v_mul_f32_e32 v147, v137, v147
	v_med3_f32 v10, v10, s60, v200
	v_med3_f32 v153, v153, s60, v200
	v_med3_f32 v203, v203, s60, v200
	v_med3_f32 v204, v204, s60, v200
	v_cvt_f32_ubyte0_e32 v206, v149
	v_cvt_f32_ubyte1_e32 v207, v149
	v_max_f32_e32 v188, 0.5, v188
	v_max_f32_e32 v146, 0.5, v146
	v_max_f32_e32 v205, 0.5, v205
	v_mul_f32_e32 v148, v109, v148
	v_med3_f32 v202, v202, s60, v200
	v_med3_f32 v147, v147, s60, v200
	v_cvt_pk_fp8_f32 v150, v10, v153
	v_cvt_pk_fp8_f32 v152, v203, v204
	v_mul_f32_e32 v188, 0x38808081, v188
	v_mul_f32_e32 v146, 0x38808081, v146
	v_mul_f32_e32 v205, 0x38808081, v205
	v_med3_f32 v10, v148, s60, v200
	v_cvt_pk_fp8_f32 v151, v202, v147 op_sel:[0,0,1]
	v_max_f32_e32 v147, 0.5, v206
	v_max_f32_e32 v148, 0.5, v207
	v_mul_f32_e32 v188, v140, v188
	v_mul_f32_e32 v146, v141, v146
	v_mul_f32_e32 v205, v108, v205
	v_mul_f32_e32 v147, 0x38808081, v147
	v_mul_f32_e32 v148, 0x38808081, v148
	v_med3_f32 v188, v188, s60, v200
	v_med3_f32 v146, v146, s60, v200
	v_med3_f32 v205, v205, s60, v200
	v_mul_f32_e32 v147, v102, v147
	v_mul_f32_e32 v148, v103, v148
	v_cvt_pk_fp8_f32 v150, v188, v146 op_sel:[0,0,1]
	v_cvt_pk_fp8_f32 v152, v205, v10 op_sel:[0,0,1]
	v_cvt_f32_ubyte2_e32 v10, v149
	v_cvt_f32_ubyte3_e32 v146, v149
	v_med3_f32 v147, v147, s60, v200
	v_med3_f32 v148, v148, s60, v200
	v_mov_b32_e32 v153, 0
	v_max_f32_e32 v10, 0.5, v10
	v_max_f32_e32 v146, 0.5, v146
	v_cvt_pk_fp8_f32 v153, v147, v148
	v_mul_f32_e32 v10, 0x38808081, v10
	v_mul_f32_e32 v146, 0x38808081, v146
	v_mul_f32_e32 v10, v104, v10
	v_mul_f32_e32 v146, v105, v146
	v_med3_f32 v10, v10, s60, v200
	v_med3_f32 v146, v146, s60, v200
	v_cvt_pk_fp8_f32 v153, v10, v146 op_sel:[0,0,1]
	v_lshrrev_b64 v[146:147], 4, v[144:145]
	v_and_b32_e32 v147, 0x1ffff, v147
	v_and_b32_e32 v146, -16, v146
	v_lshl_add_u64 v[146:147], v[146:147], 0, s[26:27]
	v_lshlrev_b64 v[146:147], 15, v[146:147]
	v_lshlrev_b32_e32 v10, 7, v144
	v_and_b32_e32 v10, 0x6780, v10
	v_lshl_add_u64 v[144:145], s[12:13], 0, v[146:147]
	v_lshl_add_u64 v[144:145], v[144:145], 0, v[10:11]
	v_lshl_add_u64 v[144:145], v[144:145], 0, v[178:179]
	global_store_dwordx4 v[144:145], v[150:153], off
	v_cvt_f32_ubyte0_e32 v10, v154
	v_cvt_f32_ubyte1_e32 v144, v154
	v_max_f32_e32 v10, 0.5, v10
	v_max_f32_e32 v144, 0.5, v144
	v_mul_f32_e32 v10, 0x38808081, v10
	v_mul_f32_e32 v144, 0x38808081, v144
	v_mul_f32_e32 v10, v130, v10
	v_mul_f32_e32 v144, v131, v144
	v_cvt_f32_ubyte2_e32 v145, v154
	v_cvt_f32_ubyte3_e32 v146, v154
	v_med3_f32 v10, v10, s60, v200
	v_med3_f32 v147, v144, s60, v200
	v_mov_b32_e32 v144, v11
	v_max_f32_e32 v145, 0.5, v145
	v_max_f32_e32 v146, 0.5, v146
	v_cvt_pk_fp8_f32 v144, v10, v147
	v_mul_f32_e32 v145, 0x38808081, v145
	v_mul_f32_e32 v146, 0x38808081, v146
	v_mul_f32_e32 v145, v132, v145
	v_mul_f32_e32 v10, v133, v146
	v_med3_f32 v145, v145, s60, v200
	v_med3_f32 v10, v10, s60, v200
	v_cvt_pk_fp8_f32 v144, v145, v10 op_sel:[0,0,1]
	v_cvt_f32_ubyte0_e32 v10, v155
	v_cvt_f32_ubyte1_e32 v145, v155
	v_max_f32_e32 v10, 0.5, v10
	v_max_f32_e32 v145, 0.5, v145
	v_mul_f32_e32 v10, 0x38808081, v10
	v_mul_f32_e32 v145, 0x38808081, v145
	v_mul_f32_e32 v10, v126, v10
	v_mul_f32_e32 v145, v127, v145
	v_cvt_f32_ubyte2_e32 v146, v155
	v_cvt_f32_ubyte3_e32 v147, v155
; __device__ __forceinline__ f32x4 u8x4_f32(unsigned w) { return (f32x4){(float)(w & 0xffu), (float)((w >> 8) & 0xffu), (float)((w >> 16) & 0xffu), (float)(w >> 24)}; }
; __device__ __forceinline__ unsigned pk4_fp8(float a, float b, float c, float d) { int w = 0; w = __builtin_amdgcn_cvt_pk_fp8_f32(clamp8(a), clamp8(b), w, false); w = __builtin_amdgcn_cvt_pk_fp8_f32(clamp8(c), clamp8(d), w, true); return (unsigned)w; }
; __host__ __device__ __forceinline__ size_t tiled_off(size_t r, int kb, int ktiles) { return (((r >> 8) * ktiles + (kb >> 7)) << 15) + ((r & 255) << 7) + (kb & 127); }
;     __device__ __forceinline__ void operator()(f32x4 (&acc)[2][2][4][2], const GUnit& u, int wr, int wc, int fr, int fq) const {
;     ...
;             for (int m = 0; m < 4; ++m) { u32x4 w;
; #pragma unroll
;                 for (int q = 0; q < 4; ++q) { const f32x4 f = u8x4_f32(qf[m][q]); const f32x4 a = acc[ai][q >> 1][m][q & 1]; f32x4 v;
; #pragma unroll
;                     for (int j = 0; j < 4; ++j) v[j] = a[j] * (fmaxf(f[j], 0.5f) * (W8_INV / 255.0f));
;                     w[q] = pk4_fp8(v[0], v[1], v[2], v[3]); }
;                 *(u32x4*)(M8 + tiled_off((size_t)(u.x0 * 256 + wr * 64 + fr + ai * 128 + m * 16), u.x1 * 256 + wc * 64 + 16 * fq, D / 128)) = w; }
	v_med3_f32 v10, v10, s60, v200
	v_med3_f32 v148, v145, s60, v200
	v_mov_b32_e32 v145, v11
	v_max_f32_e32 v146, 0.5, v146
	v_max_f32_e32 v147, 0.5, v147
	v_cvt_pk_fp8_f32 v145, v10, v148
	v_mul_f32_e32 v146, 0x38808081, v146
	v_mul_f32_e32 v147, 0x38808081, v147
	v_mul_f32_e32 v146, v128, v146
	v_mul_f32_e32 v10, v129, v147
	v_med3_f32 v146, v146, s60, v200
	v_med3_f32 v10, v10, s60, v200
	v_cvt_pk_fp8_f32 v145, v146, v10 op_sel:[0,0,1]
	v_cvt_f32_ubyte0_e32 v10, v156
	v_cvt_f32_ubyte1_e32 v146, v156
	v_max_f32_e32 v10, 0.5, v10
	v_max_f32_e32 v146, 0.5, v146
	v_mul_f32_e32 v10, 0x38808081, v10
	v_mul_f32_e32 v146, 0x38808081, v146
	v_mul_f32_e32 v10, v98, v10
	v_mul_f32_e32 v146, v99, v146
	v_cvt_f32_ubyte2_e32 v147, v156
	v_cvt_f32_ubyte3_e32 v148, v156
	v_med3_f32 v10, v10, s60, v200
	v_med3_f32 v149, v146, s60, v200
	v_mov_b32_e32 v146, v11
	v_max_f32_e32 v147, 0.5, v147
	v_max_f32_e32 v148, 0.5, v148
	v_cvt_pk_fp8_f32 v146, v10, v149
	v_mul_f32_e32 v147, 0x38808081, v147
	v_mul_f32_e32 v148, 0x38808081, v148
	v_mul_f32_e32 v147, v100, v147
	v_mul_f32_e32 v10, v101, v148
	v_med3_f32 v147, v147, s60, v200
	v_med3_f32 v10, v10, s60, v200
	v_cvt_pk_fp8_f32 v146, v147, v10 op_sel:[0,0,1]
	v_cvt_f32_ubyte0_e32 v10, v157
	v_cvt_f32_ubyte1_e32 v147, v157
	v_max_f32_e32 v10, 0.5, v10
	v_max_f32_e32 v147, 0.5, v147
	v_mul_f32_e32 v10, 0x38808081, v10
	v_mul_f32_e32 v147, 0x38808081, v147
	v_mul_f32_e32 v10, v94, v10
	v_mul_f32_e32 v147, v95, v147
	v_cvt_f32_ubyte2_e32 v148, v157
	v_cvt_f32_ubyte3_e32 v149, v157
	v_med3_f32 v10, v10, s60, v200
	v_med3_f32 v150, v147, s60, v200
	v_mov_b32_e32 v147, v11
	v_max_f32_e32 v148, 0.5, v148
	v_max_f32_e32 v149, 0.5, v149
	v_cvt_pk_fp8_f32 v147, v10, v150
	v_mul_f32_e32 v148, 0x38808081, v148
	v_mul_f32_e32 v149, 0x38808081, v149
	v_mul_f32_e32 v148, v96, v148
	v_mul_f32_e32 v10, v97, v149
	v_med3_f32 v148, v148, s60, v200
	v_med3_f32 v10, v10, s60, v200
	v_cvt_pk_fp8_f32 v147, v148, v10 op_sel:[0,0,1]
	v_add_u32_e32 v148, s28, v191
	v_ashrrev_i32_e32 v149, 31, v148
	v_lshrrev_b64 v[150:151], 4, v[148:149]
	v_and_b32_e32 v151, 0x1ffff, v151
	v_and_b32_e32 v150, -16, v150
	v_lshl_add_u64 v[150:151], v[150:151], 0, s[26:27]
	v_lshlrev_b64 v[150:151], 15, v[150:151]
	v_lshlrev_b32_e32 v10, 7, v148
	v_and_b32_e32 v10, 0x7f80, v10
	v_lshl_add_u64 v[148:149], s[12:13], 0, v[150:151]
	v_lshl_add_u64 v[148:149], v[148:149], 0, v[10:11]
	v_lshl_add_u64 v[148:149], v[148:149], 0, v[178:179]
	global_store_dwordx4 v[148:149], v[144:147], off
	v_cvt_f32_ubyte0_e32 v10, v6
	v_max_f32_e32 v10, 0.5, v10
	v_cvt_f32_ubyte1_e32 v144, v6
	v_max_f32_e32 v144, 0.5, v144
	v_cvt_f32_ubyte2_e32 v145, v6
	v_cvt_f32_ubyte3_e32 v6, v6
	v_mul_f32_e32 v10, 0x38808081, v10
	v_mul_f32_e32 v144, 0x38808081, v144
	v_mul_f32_e32 v10, v122, v10
	v_mul_f32_e32 v144, v123, v144
	v_max_f32_e32 v6, 0.5, v6
	v_mul_f32_e32 v146, 0x38808081, v6
	v_med3_f32 v10, v10, s60, v200
	v_med3_f32 v144, v144, s60, v200
	v_mov_b32_e32 v6, v11
	v_max_f32_e32 v145, 0.5, v145
	v_cvt_pk_fp8_f32 v6, v10, v144
	v_mul_f32_e32 v145, 0x38808081, v145
	v_mul_f32_e32 v145, v124, v145
	v_mul_f32_e32 v10, v125, v146
	v_med3_f32 v144, v145, s60, v200
	v_med3_f32 v10, v10, s60, v200
	v_cvt_pk_fp8_f32 v6, v144, v10 op_sel:[0,0,1]
	v_cvt_f32_ubyte0_e32 v10, v7
	v_cvt_f32_ubyte1_e32 v144, v7
	v_max_f32_e32 v10, 0.5, v10
	v_max_f32_e32 v144, 0.5, v144
	v_cvt_f32_ubyte2_e32 v145, v7
	v_cvt_f32_ubyte3_e32 v7, v7
	v_mul_f32_e32 v10, 0x38808081, v10
	v_mul_f32_e32 v144, 0x38808081, v144
	v_mul_f32_e32 v10, v118, v10
	v_mul_f32_e32 v144, v119, v144
	v_max_f32_e32 v7, 0.5, v7
	v_mul_f32_e32 v146, 0x38808081, v7
	v_med3_f32 v10, v10, s60, v200
	v_med3_f32 v144, v144, s60, v200
	v_mov_b32_e32 v7, v11
	v_max_f32_e32 v145, 0.5, v145
	v_cvt_pk_fp8_f32 v7, v10, v144
	v_mul_f32_e32 v145, 0x38808081, v145
	v_mul_f32_e32 v145, v120, v145
	v_mul_f32_e32 v10, v121, v146
	v_med3_f32 v144, v145, s60, v200
	v_med3_f32 v10, v10, s60, v200
	v_cvt_pk_fp8_f32 v7, v144, v10 op_sel:[0,0,1]
	v_cvt_f32_ubyte0_e32 v10, v8
	v_cvt_f32_ubyte1_e32 v144, v8
	v_max_f32_e32 v10, 0.5, v10
	v_max_f32_e32 v144, 0.5, v144
	v_cvt_f32_ubyte2_e32 v145, v8
	v_cvt_f32_ubyte3_e32 v8, v8
	v_mul_f32_e32 v10, 0x38808081, v10
	v_mul_f32_e32 v144, 0x38808081, v144
	v_mul_f32_e32 v10, v90, v10
	v_mul_f32_e32 v144, v91, v144
	v_max_f32_e32 v8, 0.5, v8
	v_mul_f32_e32 v146, 0x38808081, v8
	v_med3_f32 v10, v10, s60, v200
	v_med3_f32 v144, v144, s60, v200
	v_mov_b32_e32 v8, v11
	v_max_f32_e32 v145, 0.5, v145
	v_cvt_pk_fp8_f32 v8, v10, v144
	v_mul_f32_e32 v145, 0x38808081, v145
	v_mul_f32_e32 v145, v92, v145
	v_mul_f32_e32 v10, v93, v146
	v_med3_f32 v144, v145, s60, v200
	v_med3_f32 v10, v10, s60, v200
	v_cvt_pk_fp8_f32 v8, v144, v10 op_sel:[0,0,1]
	v_cvt_f32_ubyte0_e32 v10, v9
	v_cvt_f32_ubyte1_e32 v144, v9
	v_max_f32_e32 v10, 0.5, v10
	v_max_f32_e32 v144, 0.5, v144
	v_cvt_f32_ubyte2_e32 v145, v9
	v_cvt_f32_ubyte3_e32 v9, v9
	v_mul_f32_e32 v10, 0x38808081, v10
	v_mul_f32_e32 v144, 0x38808081, v144
	v_mul_f32_e32 v10, v86, v10
	v_mul_f32_e32 v144, v87, v144
	v_max_f32_e32 v9, 0.5, v9
	v_mul_f32_e32 v146, 0x38808081, v9
	v_med3_f32 v10, v10, s60, v200
	v_med3_f32 v144, v144, s60, v200
	v_mov_b32_e32 v9, v11
	v_max_f32_e32 v145, 0.5, v145
	v_cvt_pk_fp8_f32 v9, v10, v144
	v_mul_f32_e32 v145, 0x38808081, v145
	v_mul_f32_e32 v145, v88, v145
	v_mul_f32_e32 v10, v89, v146
	v_med3_f32 v144, v145, s60, v200
	v_med3_f32 v10, v10, s60, v200
	v_cvt_pk_fp8_f32 v9, v144, v10 op_sel:[0,0,1]
	v_add_u32_e32 v144, s28, v192
	v_ashrrev_i32_e32 v145, 31, v144
	v_lshrrev_b64 v[146:147], 4, v[144:145]
	v_and_b32_e32 v147, 0x1ffff, v147
; __device__ __forceinline__ f32x4 u8x4_f32(unsigned w) { return (f32x4){(float)(w & 0xffu), (float)((w >> 8) & 0xffu), (float)((w >> 16) & 0xffu), (float)(w >> 24)}; }
; __device__ __forceinline__ unsigned pk4_fp8(float a, float b, float c, float d) { int w = 0; w = __builtin_amdgcn_cvt_pk_fp8_f32(clamp8(a), clamp8(b), w, false); w = __builtin_amdgcn_cvt_pk_fp8_f32(clamp8(c), clamp8(d), w, true); return (unsigned)w; }
; __host__ __device__ __forceinline__ size_t tiled_off(size_t r, int kb, int ktiles) { return (((r >> 8) * ktiles + (kb >> 7)) << 15) + ((r & 255) << 7) + (kb & 127); }
;     __device__ __forceinline__ void operator()(f32x4 (&acc)[2][2][4][2], const GUnit& u, int wr, int wc, int fr, int fq) const {
;     ...
;         for (int ai = 0; ai < 2; ++ai) {
;             u32x4 qf[4];
; #pragma unroll
;             for (int m = 0; m < 4; ++m) qf[m] = __builtin_nontemporal_load((const u32x4*)(GZF + off0 + (size_t)(ai * 128 + m * 16) * D));
; #pragma unroll
;             for (int m = 0; m < 4; ++m) { u32x4 w;
; #pragma unroll
;                 for (int q = 0; q < 4; ++q) { const f32x4 f = u8x4_f32(qf[m][q]); const f32x4 a = acc[ai][q >> 1][m][q & 1]; f32x4 v;
; #pragma unroll
;                     for (int j = 0; j < 4; ++j) v[j] = a[j] * (fmaxf(f[j], 0.5f) * (W8_INV / 255.0f));
;                     w[q] = pk4_fp8(v[0], v[1], v[2], v[3]); }
;                 *(u32x4*)(M8 + tiled_off((size_t)(u.x0 * 256 + wr * 64 + fr + ai * 128 + m * 16), u.x1 * 256 + wc * 64 + 16 * fq, D / 128)) = w; }
	v_and_b32_e32 v146, -16, v146
	v_lshl_add_u64 v[146:147], v[146:147], 0, s[26:27]
	v_lshlrev_b64 v[146:147], 15, v[146:147]
	v_lshlrev_b32_e32 v10, 7, v144
	v_and_b32_e32 v10, 0x7f80, v10
	v_lshl_add_u64 v[144:145], s[12:13], 0, v[146:147]
	v_lshl_add_u64 v[144:145], v[144:145], 0, v[10:11]
	v_lshl_add_u64 v[144:145], v[144:145], 0, v[178:179]
	global_store_dwordx4 v[144:145], v[6:9], off
	s_nop 1
	v_cvt_f32_ubyte0_e32 v6, v2
	v_cvt_f32_ubyte1_e32 v7, v2
	v_max_f32_e32 v6, 0.5, v6
	v_max_f32_e32 v7, 0.5, v7
	v_cvt_f32_ubyte2_e32 v8, v2
	v_cvt_f32_ubyte3_e32 v2, v2
	v_mul_f32_e32 v6, 0x38808081, v6
	v_mul_f32_e32 v7, 0x38808081, v7
	v_mul_f32_e32 v6, v114, v6
	v_mul_f32_e32 v7, v115, v7
	v_max_f32_e32 v2, 0.5, v2
	v_mul_f32_e32 v9, 0x38808081, v2
	v_med3_f32 v6, v6, s60, v200
	v_med3_f32 v7, v7, s60, v200
	v_mov_b32_e32 v2, v11
	v_max_f32_e32 v8, 0.5, v8
	v_cvt_pk_fp8_f32 v2, v6, v7
	v_mul_f32_e32 v8, 0x38808081, v8
	v_mul_f32_e32 v8, v116, v8
	v_mul_f32_e32 v6, v117, v9
	v_med3_f32 v7, v8, s60, v200
	v_med3_f32 v6, v6, s60, v200
	v_cvt_pk_fp8_f32 v2, v7, v6 op_sel:[0,0,1]
	v_cvt_f32_ubyte0_e32 v6, v3
	v_cvt_f32_ubyte1_e32 v7, v3
	v_max_f32_e32 v6, 0.5, v6
	v_max_f32_e32 v7, 0.5, v7
	v_cvt_f32_ubyte2_e32 v8, v3
	v_cvt_f32_ubyte3_e32 v3, v3
	v_mul_f32_e32 v6, 0x38808081, v6
	v_mul_f32_e32 v7, 0x38808081, v7
	v_mul_f32_e32 v6, v110, v6
	v_mul_f32_e32 v7, v111, v7
	v_max_f32_e32 v3, 0.5, v3
	v_mul_f32_e32 v9, 0x38808081, v3
	v_med3_f32 v6, v6, s60, v200
	v_med3_f32 v7, v7, s60, v200
	v_mov_b32_e32 v3, v11
	v_max_f32_e32 v8, 0.5, v8
	v_cvt_pk_fp8_f32 v3, v6, v7
	v_mul_f32_e32 v8, 0x38808081, v8
	v_mul_f32_e32 v8, v112, v8
	v_mul_f32_e32 v6, v113, v9
	v_med3_f32 v7, v8, s60, v200
	v_med3_f32 v6, v6, s60, v200
	v_cvt_pk_fp8_f32 v3, v7, v6 op_sel:[0,0,1]
	v_cvt_f32_ubyte0_e32 v6, v4
	v_cvt_f32_ubyte1_e32 v7, v4
	v_max_f32_e32 v6, 0.5, v6
	v_max_f32_e32 v7, 0.5, v7
	v_cvt_f32_ubyte2_e32 v8, v4
	v_cvt_f32_ubyte3_e32 v4, v4
	v_mul_f32_e32 v6, 0x38808081, v6
	v_mul_f32_e32 v7, 0x38808081, v7
	v_mul_f32_e32 v6, v82, v6
	v_mul_f32_e32 v7, v83, v7
	v_max_f32_e32 v4, 0.5, v4
	v_mul_f32_e32 v9, 0x38808081, v4
	v_med3_f32 v6, v6, s60, v200
	v_med3_f32 v7, v7, s60, v200
	v_mov_b32_e32 v4, v11
	v_max_f32_e32 v8, 0.5, v8
	v_cvt_pk_fp8_f32 v4, v6, v7
	v_mul_f32_e32 v8, 0x38808081, v8
	v_mul_f32_e32 v8, v84, v8
	v_mul_f32_e32 v6, v85, v9
	v_med3_f32 v7, v8, s60, v200
	v_med3_f32 v6, v6, s60, v200
	v_cvt_pk_fp8_f32 v4, v7, v6 op_sel:[0,0,1]
	v_cvt_f32_ubyte0_e32 v6, v5
	v_cvt_f32_ubyte1_e32 v7, v5
	v_max_f32_e32 v6, 0.5, v6
	v_max_f32_e32 v7, 0.5, v7
	v_cvt_f32_ubyte2_e32 v8, v5
	v_cvt_f32_ubyte3_e32 v5, v5
	v_mul_f32_e32 v6, 0x38808081, v6
	v_mul_f32_e32 v7, 0x38808081, v7
	v_mul_f32_e32 v6, v78, v6
	v_mul_f32_e32 v7, v79, v7
	v_max_f32_e32 v5, 0.5, v5
	v_mul_f32_e32 v9, 0x38808081, v5
	v_med3_f32 v6, v6, s60, v200
	v_med3_f32 v7, v7, s60, v200
	v_mov_b32_e32 v5, v11
	v_max_f32_e32 v8, 0.5, v8
	v_cvt_pk_fp8_f32 v5, v6, v7
	v_mul_f32_e32 v8, 0x38808081, v8
	v_mul_f32_e32 v8, v80, v8
	v_mul_f32_e32 v6, v81, v9
	v_med3_f32 v7, v8, s60, v200
	v_med3_f32 v6, v6, s60, v200
	v_cvt_pk_fp8_f32 v5, v7, v6 op_sel:[0,0,1]
	v_add_u32_e32 v6, s28, v193
	v_ashrrev_i32_e32 v7, 31, v6
	v_lshrrev_b64 v[8:9], 4, v[6:7]
	v_and_b32_e32 v9, 0x1ffff, v9
	v_and_b32_e32 v8, -16, v8
	v_lshl_add_u64 v[8:9], v[8:9], 0, s[26:27]
	v_lshlrev_b64 v[8:9], 15, v[8:9]
	v_lshlrev_b32_e32 v6, 7, v6
	v_and_b32_e32 v10, 0x7f80, v6
	v_lshl_add_u64 v[6:7], s[12:13], 0, v[8:9]
	v_lshl_add_u64 v[6:7], v[6:7], 0, v[10:11]
	v_lshl_add_u64 v[6:7], v[6:7], 0, v[178:179]
	global_store_dwordx4 v[6:7], v[2:5], off
	s_nop 1
	v_add_co_u32_e32 v2, vcc, s61, v12
	s_nop 1
	v_addc_co_u32_e32 v3, vcc, 0, v13, vcc
	global_load_dwordx4 v[144:147], v[2:3], off nt
	v_add_co_u32_e32 v2, vcc, s62, v12
	s_waitcnt vmcnt(0) lgkmcnt(0)
	v_cvt_f32_ubyte0_e32 v10, v144
	v_addc_co_u32_e32 v3, vcc, 0, v13, vcc
	global_load_dwordx4 v[148:151], v[2:3], off nt
	v_cvt_f32_ubyte1_e32 v152, v144
	v_max_f32_e32 v10, 0.5, v10
	v_max_f32_e32 v152, 0.5, v152
	v_cvt_f32_ubyte2_e32 v153, v144
	v_cvt_f32_ubyte3_e32 v144, v144
	v_mul_f32_e32 v10, 0x38808081, v10
	v_mul_f32_e32 v152, 0x38808081, v152
	v_mul_f32_e32 v10, v74, v10
	v_mul_f32_e32 v152, v75, v152
	v_max_f32_e32 v144, 0.5, v144
	v_mul_f32_e32 v154, 0x38808081, v144
	v_med3_f32 v10, v10, s60, v200
	v_med3_f32 v152, v152, s60, v200
	v_mov_b32_e32 v144, v11
	v_max_f32_e32 v153, 0.5, v153
	v_cvt_pk_fp8_f32 v144, v10, v152
	v_mul_f32_e32 v153, 0x38808081, v153
	v_add_co_u32_e32 v2, vcc, s63, v12
	v_mul_f32_e32 v153, v76, v153
	v_mul_f32_e32 v10, v77, v154
	v_addc_co_u32_e32 v3, vcc, 0, v13, vcc
	v_med3_f32 v152, v153, s60, v200
	v_med3_f32 v10, v10, s60, v200
	v_add_co_u32_e32 v4, vcc, s64, v12
	v_cvt_pk_fp8_f32 v144, v152, v10 op_sel:[0,0,1]
	v_cvt_f32_ubyte0_e32 v10, v145
	v_cvt_f32_ubyte1_e32 v152, v145
	v_addc_co_u32_e32 v5, vcc, 0, v13, vcc
	v_max_f32_e32 v10, 0.5, v10
	v_max_f32_e32 v152, 0.5, v152
	global_load_dwordx4 v[6:9], v[2:3], off nt
	s_nop 0
	global_load_dwordx4 v[2:5], v[4:5], off nt
	v_cvt_f32_ubyte2_e32 v153, v145
	v_cvt_f32_ubyte3_e32 v145, v145
	v_mul_f32_e32 v10, 0x38808081, v10
	v_mul_f32_e32 v152, 0x38808081, v152
	v_mul_f32_e32 v10, v70, v10
	v_mul_f32_e32 v152, v71, v152
	v_max_f32_e32 v145, 0.5, v145
	v_mul_f32_e32 v154, 0x38808081, v145
	v_med3_f32 v10, v10, s60, v200
	v_med3_f32 v152, v152, s60, v200
	v_mov_b32_e32 v145, v11
	v_max_f32_e32 v153, 0.5, v153
	v_cvt_pk_fp8_f32 v145, v10, v152
	v_mul_f32_e32 v153, 0x38808081, v153
	v_mul_f32_e32 v153, v72, v153
	v_mul_f32_e32 v10, v73, v154
	v_med3_f32 v152, v153, s60, v200
	v_med3_f32 v10, v10, s60, v200
; __device__ __forceinline__ f32x4 u8x4_f32(unsigned w) { return (f32x4){(float)(w & 0xffu), (float)((w >> 8) & 0xffu), (float)((w >> 16) & 0xffu), (float)(w >> 24)}; }
; __device__ __forceinline__ unsigned pk4_fp8(float a, float b, float c, float d) { int w = 0; w = __builtin_amdgcn_cvt_pk_fp8_f32(clamp8(a), clamp8(b), w, false); w = __builtin_amdgcn_cvt_pk_fp8_f32(clamp8(c), clamp8(d), w, true); return (unsigned)w; }
; __host__ __device__ __forceinline__ size_t tiled_off(size_t r, int kb, int ktiles) { return (((r >> 8) * ktiles + (kb >> 7)) << 15) + ((r & 255) << 7) + (kb & 127); }
;     __device__ __forceinline__ void operator()(f32x4 (&acc)[2][2][4][2], const GUnit& u, int wr, int wc, int fr, int fq) const {
;     ...
;             for (int m = 0; m < 4; ++m) { u32x4 w;
; #pragma unroll
;                 for (int q = 0; q < 4; ++q) { const f32x4 f = u8x4_f32(qf[m][q]); const f32x4 a = acc[ai][q >> 1][m][q & 1]; f32x4 v;
; #pragma unroll
;                     for (int j = 0; j < 4; ++j) v[j] = a[j] * (fmaxf(f[j], 0.5f) * (W8_INV / 255.0f));
;                     w[q] = pk4_fp8(v[0], v[1], v[2], v[3]); }
;                 *(u32x4*)(M8 + tiled_off((size_t)(u.x0 * 256 + wr * 64 + fr + ai * 128 + m * 16), u.x1 * 256 + wc * 64 + 16 * fq, D / 128)) = w; }
	v_cvt_pk_fp8_f32 v145, v152, v10 op_sel:[0,0,1]
	v_cvt_f32_ubyte0_e32 v10, v146
	v_cvt_f32_ubyte1_e32 v152, v146
	v_max_f32_e32 v10, 0.5, v10
	v_max_f32_e32 v152, 0.5, v152
	v_cvt_f32_ubyte2_e32 v153, v146
	v_cvt_f32_ubyte3_e32 v146, v146
	v_mul_f32_e32 v10, 0x38808081, v10
	v_mul_f32_e32 v152, 0x38808081, v152
	v_mul_f32_e32 v10, v42, v10
	v_mul_f32_e32 v152, v43, v152
	v_max_f32_e32 v146, 0.5, v146
	v_mul_f32_e32 v154, 0x38808081, v146
	v_med3_f32 v10, v10, s60, v200
	v_med3_f32 v152, v152, s60, v200
	v_mov_b32_e32 v146, v11
	v_max_f32_e32 v153, 0.5, v153
	v_cvt_pk_fp8_f32 v146, v10, v152
	v_mul_f32_e32 v153, 0x38808081, v153
	v_mul_f32_e32 v153, v44, v153
	v_mul_f32_e32 v10, v45, v154
	v_med3_f32 v152, v153, s60, v200
	v_med3_f32 v10, v10, s60, v200
	v_cvt_pk_fp8_f32 v146, v152, v10 op_sel:[0,0,1]
	v_cvt_f32_ubyte0_e32 v10, v147
	v_cvt_f32_ubyte1_e32 v152, v147
	v_max_f32_e32 v10, 0.5, v10
	v_max_f32_e32 v152, 0.5, v152
	v_cvt_f32_ubyte2_e32 v153, v147
	v_cvt_f32_ubyte3_e32 v147, v147
	v_mul_f32_e32 v10, 0x38808081, v10
	v_mul_f32_e32 v152, 0x38808081, v152
	v_mul_f32_e32 v10, v38, v10
	v_mul_f32_e32 v152, v39, v152
	v_max_f32_e32 v147, 0.5, v147
	v_mul_f32_e32 v154, 0x38808081, v147
	v_med3_f32 v10, v10, s60, v200
	v_med3_f32 v152, v152, s60, v200
	v_mov_b32_e32 v147, v11
	v_max_f32_e32 v153, 0.5, v153
	v_cvt_pk_fp8_f32 v147, v10, v152
	v_mul_f32_e32 v153, 0x38808081, v153
	v_mul_f32_e32 v153, v40, v153
	v_mul_f32_e32 v10, v41, v154
	v_med3_f32 v152, v153, s60, v200
	v_med3_f32 v10, v10, s60, v200
	v_cvt_pk_fp8_f32 v147, v152, v10 op_sel:[0,0,1]
	v_add_u32_e32 v152, s28, v194
	v_ashrrev_i32_e32 v153, 31, v152
	v_lshrrev_b64 v[154:155], 4, v[152:153]
	v_and_b32_e32 v155, 0x1ffff, v155
	v_and_b32_e32 v154, -16, v154
	v_lshl_add_u64 v[154:155], v[154:155], 0, s[26:27]
	v_lshlrev_b64 v[154:155], 15, v[154:155]
	v_lshlrev_b32_e32 v10, 7, v152
	v_and_b32_e32 v10, 0x7f80, v10
	v_lshl_add_u64 v[152:153], s[12:13], 0, v[154:155]
	v_lshl_add_u64 v[152:153], v[152:153], 0, v[10:11]
	v_lshl_add_u64 v[152:153], v[152:153], 0, v[178:179]
	global_store_dwordx4 v[152:153], v[144:147], off
	s_waitcnt vmcnt(0) lgkmcnt(0)
	v_cvt_f32_ubyte0_e32 v10, v148
	v_max_f32_e32 v10, 0.5, v10
	v_cvt_f32_ubyte1_e32 v144, v148
	v_max_f32_e32 v144, 0.5, v144
	v_mul_f32_e32 v10, 0x38808081, v10
	v_mul_f32_e32 v144, 0x38808081, v144
	v_mul_f32_e32 v10, v66, v10
	v_mul_f32_e32 v144, v67, v144
	v_cvt_f32_ubyte2_e32 v145, v148
	v_cvt_f32_ubyte3_e32 v146, v148
	v_med3_f32 v10, v10, s60, v200
	v_med3_f32 v147, v144, s60, v200
	v_mov_b32_e32 v144, v11
	v_max_f32_e32 v145, 0.5, v145
	v_max_f32_e32 v146, 0.5, v146
	v_cvt_pk_fp8_f32 v144, v10, v147
	v_mul_f32_e32 v145, 0x38808081, v145
	v_mul_f32_e32 v146, 0x38808081, v146
	v_mul_f32_e32 v145, v68, v145
	v_mul_f32_e32 v10, v69, v146
	v_med3_f32 v145, v145, s60, v200
	v_med3_f32 v10, v10, s60, v200
	v_cvt_pk_fp8_f32 v144, v145, v10 op_sel:[0,0,1]
	v_cvt_f32_ubyte0_e32 v10, v149
	v_cvt_f32_ubyte1_e32 v145, v149
	v_max_f32_e32 v10, 0.5, v10
	v_max_f32_e32 v145, 0.5, v145
	v_mul_f32_e32 v10, 0x38808081, v10
	v_mul_f32_e32 v145, 0x38808081, v145
	v_mul_f32_e32 v10, v62, v10
	v_mul_f32_e32 v145, v63, v145
	v_cvt_f32_ubyte2_e32 v146, v149
	v_cvt_f32_ubyte3_e32 v147, v149
	v_med3_f32 v10, v10, s60, v200
	v_med3_f32 v148, v145, s60, v200
	v_mov_b32_e32 v145, v11
	v_max_f32_e32 v146, 0.5, v146
	v_max_f32_e32 v147, 0.5, v147
	v_cvt_pk_fp8_f32 v145, v10, v148
	v_mul_f32_e32 v146, 0x38808081, v146
	v_mul_f32_e32 v147, 0x38808081, v147
	v_mul_f32_e32 v146, v64, v146
	v_mul_f32_e32 v10, v65, v147
	v_med3_f32 v146, v146, s60, v200
	v_med3_f32 v10, v10, s60, v200
	v_cvt_pk_fp8_f32 v145, v146, v10 op_sel:[0,0,1]
	v_cvt_f32_ubyte0_e32 v10, v150
	v_cvt_f32_ubyte1_e32 v146, v150
	v_max_f32_e32 v10, 0.5, v10
	v_max_f32_e32 v146, 0.5, v146
	v_mul_f32_e32 v10, 0x38808081, v10
	v_mul_f32_e32 v146, 0x38808081, v146
	v_mul_f32_e32 v10, v34, v10
	v_mul_f32_e32 v146, v35, v146
	v_cvt_f32_ubyte2_e32 v147, v150
	v_cvt_f32_ubyte3_e32 v148, v150
	v_med3_f32 v10, v10, s60, v200
	v_med3_f32 v149, v146, s60, v200
	v_mov_b32_e32 v146, v11
	v_max_f32_e32 v147, 0.5, v147
	v_max_f32_e32 v148, 0.5, v148
	v_cvt_pk_fp8_f32 v146, v10, v149
	v_mul_f32_e32 v147, 0x38808081, v147
	v_mul_f32_e32 v148, 0x38808081, v148
	v_mul_f32_e32 v147, v36, v147
	v_mul_f32_e32 v10, v37, v148
	v_med3_f32 v147, v147, s60, v200
	v_med3_f32 v10, v10, s60, v200
	v_cvt_pk_fp8_f32 v146, v147, v10 op_sel:[0,0,1]
	v_cvt_f32_ubyte0_e32 v10, v151
	v_cvt_f32_ubyte1_e32 v147, v151
	v_max_f32_e32 v10, 0.5, v10
	v_max_f32_e32 v147, 0.5, v147
	v_mul_f32_e32 v10, 0x38808081, v10
	v_mul_f32_e32 v147, 0x38808081, v147
	v_mul_f32_e32 v10, v30, v10
	v_mul_f32_e32 v147, v31, v147
	v_cvt_f32_ubyte2_e32 v148, v151
	v_cvt_f32_ubyte3_e32 v149, v151
	v_med3_f32 v10, v10, s60, v200
	v_med3_f32 v150, v147, s60, v200
	v_mov_b32_e32 v147, v11
	v_max_f32_e32 v148, 0.5, v148
	v_max_f32_e32 v149, 0.5, v149
	v_cvt_pk_fp8_f32 v147, v10, v150
	v_mul_f32_e32 v148, 0x38808081, v148
	v_mul_f32_e32 v149, 0x38808081, v149
	v_mul_f32_e32 v148, v32, v148
	v_mul_f32_e32 v10, v33, v149
	v_med3_f32 v148, v148, s60, v200
	v_med3_f32 v10, v10, s60, v200
	v_cvt_pk_fp8_f32 v147, v148, v10 op_sel:[0,0,1]
	v_add_u32_e32 v148, s28, v195
	v_ashrrev_i32_e32 v149, 31, v148
	v_lshrrev_b64 v[150:151], 4, v[148:149]
	v_and_b32_e32 v151, 0x1ffff, v151
	v_and_b32_e32 v150, -16, v150
	v_lshl_add_u64 v[150:151], v[150:151], 0, s[26:27]
	v_lshlrev_b64 v[150:151], 15, v[150:151]
	v_lshlrev_b32_e32 v10, 7, v148
	v_and_b32_e32 v10, 0x7f80, v10
	v_lshl_add_u64 v[148:149], s[12:13], 0, v[150:151]
	v_lshl_add_u64 v[148:149], v[148:149], 0, v[10:11]
; __device__ __forceinline__ f32x4 u8x4_f32(unsigned w) { return (f32x4){(float)(w & 0xffu), (float)((w >> 8) & 0xffu), (float)((w >> 16) & 0xffu), (float)(w >> 24)}; }
; __device__ __forceinline__ unsigned pk4_fp8(float a, float b, float c, float d) { int w = 0; w = __builtin_amdgcn_cvt_pk_fp8_f32(clamp8(a), clamp8(b), w, false); w = __builtin_amdgcn_cvt_pk_fp8_f32(clamp8(c), clamp8(d), w, true); return (unsigned)w; }
; __host__ __device__ __forceinline__ size_t tiled_off(size_t r, int kb, int ktiles) { return (((r >> 8) * ktiles + (kb >> 7)) << 15) + ((r & 255) << 7) + (kb & 127); }
;     __device__ __forceinline__ void operator()(f32x4 (&acc)[2][2][4][2], const GUnit& u, int wr, int wc, int fr, int fq) const {
;     ...
;             for (int m = 0; m < 4; ++m) { u32x4 w;
; #pragma unroll
;                 for (int q = 0; q < 4; ++q) { const f32x4 f = u8x4_f32(qf[m][q]); const f32x4 a = acc[ai][q >> 1][m][q & 1]; f32x4 v;
; #pragma unroll
;                     for (int j = 0; j < 4; ++j) v[j] = a[j] * (fmaxf(f[j], 0.5f) * (W8_INV / 255.0f));
;                     w[q] = pk4_fp8(v[0], v[1], v[2], v[3]); }
;                 *(u32x4*)(M8 + tiled_off((size_t)(u.x0 * 256 + wr * 64 + fr + ai * 128 + m * 16), u.x1 * 256 + wc * 64 + 16 * fq, D / 128)) = w; }
;             asm volatile("" ::: "memory");
;         }
;     }
	v_lshl_add_u64 v[148:149], v[148:149], 0, v[178:179]
	global_store_dwordx4 v[148:149], v[144:147], off
	v_cvt_f32_ubyte0_e32 v10, v6
	v_max_f32_e32 v10, 0.5, v10
	v_cvt_f32_ubyte1_e32 v144, v6
	v_max_f32_e32 v144, 0.5, v144
	v_cvt_f32_ubyte2_e32 v145, v6
	v_cvt_f32_ubyte3_e32 v6, v6
	v_mul_f32_e32 v10, 0x38808081, v10
	v_mul_f32_e32 v144, 0x38808081, v144
	v_mul_f32_e32 v10, v58, v10
	v_mul_f32_e32 v144, v59, v144
	v_max_f32_e32 v6, 0.5, v6
	v_mul_f32_e32 v146, 0x38808081, v6
	v_med3_f32 v10, v10, s60, v200
	v_med3_f32 v144, v144, s60, v200
	v_mov_b32_e32 v6, v11
	v_max_f32_e32 v145, 0.5, v145
	v_cvt_pk_fp8_f32 v6, v10, v144
	v_mul_f32_e32 v145, 0x38808081, v145
	v_mul_f32_e32 v145, v60, v145
	v_mul_f32_e32 v10, v61, v146
	v_med3_f32 v144, v145, s60, v200
	v_med3_f32 v10, v10, s60, v200
	v_cvt_pk_fp8_f32 v6, v144, v10 op_sel:[0,0,1]
	v_cvt_f32_ubyte0_e32 v10, v7
	v_cvt_f32_ubyte1_e32 v144, v7
	v_max_f32_e32 v10, 0.5, v10
	v_max_f32_e32 v144, 0.5, v144
	v_cvt_f32_ubyte2_e32 v145, v7
	v_cvt_f32_ubyte3_e32 v7, v7
	v_mul_f32_e32 v10, 0x38808081, v10
	v_mul_f32_e32 v144, 0x38808081, v144
	v_mul_f32_e32 v10, v54, v10
	v_mul_f32_e32 v144, v55, v144
	v_max_f32_e32 v7, 0.5, v7
	v_mul_f32_e32 v146, 0x38808081, v7
	v_med3_f32 v10, v10, s60, v200
	v_med3_f32 v144, v144, s60, v200
	v_mov_b32_e32 v7, v11
	v_max_f32_e32 v145, 0.5, v145
	v_cvt_pk_fp8_f32 v7, v10, v144
	v_mul_f32_e32 v145, 0x38808081, v145
	v_mul_f32_e32 v145, v56, v145
	v_mul_f32_e32 v10, v57, v146
	v_med3_f32 v144, v145, s60, v200
	v_med3_f32 v10, v10, s60, v200
	v_cvt_pk_fp8_f32 v7, v144, v10 op_sel:[0,0,1]
	v_cvt_f32_ubyte0_e32 v10, v8
	v_cvt_f32_ubyte1_e32 v144, v8
	v_max_f32_e32 v10, 0.5, v10
	v_max_f32_e32 v144, 0.5, v144
	v_cvt_f32_ubyte2_e32 v145, v8
	v_cvt_f32_ubyte3_e32 v8, v8
	v_mul_f32_e32 v10, 0x38808081, v10
	v_mul_f32_e32 v144, 0x38808081, v144
	v_mul_f32_e32 v10, v26, v10
	v_mul_f32_e32 v144, v27, v144
	v_max_f32_e32 v8, 0.5, v8
	v_mul_f32_e32 v146, 0x38808081, v8
	v_med3_f32 v10, v10, s60, v200
	v_med3_f32 v144, v144, s60, v200
	v_mov_b32_e32 v8, v11
	v_max_f32_e32 v145, 0.5, v145
	v_cvt_pk_fp8_f32 v8, v10, v144
	v_mul_f32_e32 v145, 0x38808081, v145
	v_mul_f32_e32 v145, v28, v145
	v_mul_f32_e32 v10, v29, v146
	v_med3_f32 v144, v145, s60, v200
	v_med3_f32 v10, v10, s60, v200
	v_cvt_pk_fp8_f32 v8, v144, v10 op_sel:[0,0,1]
	v_cvt_f32_ubyte0_e32 v10, v9
	v_cvt_f32_ubyte1_e32 v144, v9
	v_max_f32_e32 v10, 0.5, v10
	v_max_f32_e32 v144, 0.5, v144
	v_cvt_f32_ubyte2_e32 v145, v9
	v_cvt_f32_ubyte3_e32 v9, v9
	v_mul_f32_e32 v10, 0x38808081, v10
	v_mul_f32_e32 v144, 0x38808081, v144
	v_mul_f32_e32 v10, v22, v10
	v_mul_f32_e32 v144, v23, v144
	v_max_f32_e32 v9, 0.5, v9
	v_mul_f32_e32 v146, 0x38808081, v9
	v_med3_f32 v10, v10, s60, v200
	v_med3_f32 v144, v144, s60, v200
	v_mov_b32_e32 v9, v11
	v_max_f32_e32 v145, 0.5, v145
	v_cvt_pk_fp8_f32 v9, v10, v144
	v_mul_f32_e32 v145, 0x38808081, v145
	v_mul_f32_e32 v145, v24, v145
	v_mul_f32_e32 v10, v25, v146
	v_med3_f32 v144, v145, s60, v200
	v_med3_f32 v10, v10, s60, v200
	v_cvt_pk_fp8_f32 v9, v144, v10 op_sel:[0,0,1]
	v_add_u32_e32 v144, s28, v196
	v_ashrrev_i32_e32 v145, 31, v144
	v_lshrrev_b64 v[146:147], 4, v[144:145]
	v_and_b32_e32 v147, 0x1ffff, v147
	v_and_b32_e32 v146, -16, v146
	v_lshl_add_u64 v[146:147], v[146:147], 0, s[26:27]
	v_lshlrev_b64 v[146:147], 15, v[146:147]
	v_lshlrev_b32_e32 v10, 7, v144
	v_and_b32_e32 v10, 0x7f80, v10
	v_lshl_add_u64 v[144:145], s[12:13], 0, v[146:147]
	v_lshl_add_u64 v[144:145], v[144:145], 0, v[10:11]
	v_lshl_add_u64 v[144:145], v[144:145], 0, v[178:179]
	global_store_dwordx4 v[144:145], v[6:9], off
	s_nop 1
	v_cvt_f32_ubyte0_e32 v6, v2
	v_cvt_f32_ubyte1_e32 v7, v2
	v_max_f32_e32 v6, 0.5, v6
	v_max_f32_e32 v7, 0.5, v7
	v_cvt_f32_ubyte2_e32 v8, v2
	v_cvt_f32_ubyte3_e32 v2, v2
	v_mul_f32_e32 v6, 0x38808081, v6
	v_mul_f32_e32 v7, 0x38808081, v7
	v_mul_f32_e32 v6, v50, v6
	v_mul_f32_e32 v7, v51, v7
	v_max_f32_e32 v2, 0.5, v2
	v_mul_f32_e32 v9, 0x38808081, v2
	v_med3_f32 v6, v6, s60, v200
	v_med3_f32 v7, v7, s60, v200
	v_mov_b32_e32 v2, v11
	v_max_f32_e32 v8, 0.5, v8
	v_cvt_pk_fp8_f32 v2, v6, v7
	v_mul_f32_e32 v8, 0x38808081, v8
	v_mul_f32_e32 v8, v52, v8
	v_mul_f32_e32 v6, v53, v9
	v_med3_f32 v7, v8, s60, v200
	v_med3_f32 v6, v6, s60, v200
	v_cvt_pk_fp8_f32 v2, v7, v6 op_sel:[0,0,1]
	v_cvt_f32_ubyte0_e32 v6, v3
	v_cvt_f32_ubyte1_e32 v7, v3
	v_max_f32_e32 v6, 0.5, v6
	v_max_f32_e32 v7, 0.5, v7
	v_cvt_f32_ubyte2_e32 v8, v3
	v_cvt_f32_ubyte3_e32 v3, v3
	v_mul_f32_e32 v6, 0x38808081, v6
	v_mul_f32_e32 v7, 0x38808081, v7
	v_mul_f32_e32 v6, v46, v6
	v_mul_f32_e32 v7, v47, v7
	v_max_f32_e32 v3, 0.5, v3
	v_mul_f32_e32 v9, 0x38808081, v3
	v_med3_f32 v6, v6, s60, v200
	v_med3_f32 v7, v7, s60, v200
	v_mov_b32_e32 v3, v11
	v_max_f32_e32 v8, 0.5, v8
	v_cvt_pk_fp8_f32 v3, v6, v7
	v_mul_f32_e32 v8, 0x38808081, v8
	v_mul_f32_e32 v8, v48, v8
	v_mul_f32_e32 v6, v49, v9
	v_med3_f32 v7, v8, s60, v200
	v_med3_f32 v6, v6, s60, v200
	v_cvt_pk_fp8_f32 v3, v7, v6 op_sel:[0,0,1]
	v_cvt_f32_ubyte0_e32 v6, v4
	v_cvt_f32_ubyte1_e32 v7, v4
	v_max_f32_e32 v6, 0.5, v6
	v_max_f32_e32 v7, 0.5, v7
	v_cvt_f32_ubyte2_e32 v8, v4
	v_cvt_f32_ubyte3_e32 v4, v4
	v_mul_f32_e32 v6, 0x38808081, v6
	v_mul_f32_e32 v7, 0x38808081, v7
	v_mul_f32_e32 v6, v18, v6
	v_mul_f32_e32 v7, v19, v7
	v_max_f32_e32 v4, 0.5, v4
	v_mul_f32_e32 v9, 0x38808081, v4
	v_med3_f32 v6, v6, s60, v200
	v_med3_f32 v7, v7, s60, v200
	v_mov_b32_e32 v4, v11
	v_max_f32_e32 v8, 0.5, v8
	v_cvt_pk_fp8_f32 v4, v6, v7
	v_mul_f32_e32 v8, 0x38808081, v8
	v_mul_f32_e32 v8, v20, v8
	v_mul_f32_e32 v6, v21, v9
	v_med3_f32 v7, v8, s60, v200
	v_med3_f32 v6, v6, s60, v200
	v_cvt_pk_fp8_f32 v4, v7, v6 op_sel:[0,0,1]
	v_cvt_f32_ubyte0_e32 v6, v5
	v_cvt_f32_ubyte1_e32 v7, v5
	v_max_f32_e32 v6, 0.5, v6
	v_max_f32_e32 v7, 0.5, v7
	v_cvt_f32_ubyte2_e32 v8, v5
	v_cvt_f32_ubyte3_e32 v5, v5
	v_mul_f32_e32 v6, 0x38808081, v6
	v_mul_f32_e32 v7, 0x38808081, v7
	v_mul_f32_e32 v6, v14, v6
	v_mul_f32_e32 v7, v15, v7
	v_max_f32_e32 v5, 0.5, v5
	v_mul_f32_e32 v9, 0x38808081, v5
	v_med3_f32 v6, v6, s60, v200
	v_med3_f32 v7, v7, s60, v200
	v_mov_b32_e32 v5, v11
	v_max_f32_e32 v8, 0.5, v8
	v_cvt_pk_fp8_f32 v5, v6, v7
	v_mul_f32_e32 v8, 0x38808081, v8
	v_mul_f32_e32 v8, v16, v8
	v_mul_f32_e32 v6, v17, v9
	v_med3_f32 v7, v8, s60, v200
	v_med3_f32 v6, v6, s60, v200
	v_cvt_pk_fp8_f32 v5, v7, v6 op_sel:[0,0,1]
	v_add_u32_e32 v6, s28, v197
	v_ashrrev_i32_e32 v7, 31, v6
	v_lshrrev_b64 v[8:9], 4, v[6:7]
	v_and_b32_e32 v9, 0x1ffff, v9
	v_and_b32_e32 v8, -16, v8
	v_lshl_add_u64 v[8:9], v[8:9], 0, s[26:27]
	v_lshlrev_b64 v[8:9], 15, v[8:9]
	v_lshlrev_b32_e32 v6, 7, v6
	v_and_b32_e32 v10, 0x7f80, v6
	v_lshl_add_u64 v[6:7], s[12:13], 0, v[8:9]
	v_lshl_add_u64 v[6:7], v[6:7], 0, v[10:11]
	v_lshl_add_u64 v[6:7], v[6:7], 0, v[178:179]
	global_store_dwordx4 v[6:7], v[2:5], off
	s_cbranch_execnz .LBB0_840

; __device__ __forceinline__ unsigned pk4_fp8(float a, float b, float c, float d) { int w = 0; w = __builtin_amdgcn_cvt_pk_fp8_f32(clamp8(a), clamp8(b), w, false); w = __builtin_amdgcn_cvt_pk_fp8_f32(clamp8(c), clamp8(d), w, true); return (unsigned)w; }
;     __device__ __forceinline__ void operator()(AccRef acc, const GUnit& u, int wr, int wc, int fr, int fq) const {
;         const int pm = u.x0, pn = u.x1; const float* gate = modv + (size_t)(pm >> 5) * 12288 + 2 * D;
;         const int col0 = pn * 256 + wc * 64 + 16 * fq;
;         f32x4 gv[4];
; #pragma unroll
;         for (int q = 0; q < 4; ++q) gv[q] = *(const f32x4*)(gate + col0 + 4 * q) * (W8_INV * MG8_SCALE);
; #pragma unroll
;         for (int ai = 0; ai < 2; ++ai)
; #pragma unroll
;             for (int m = 0; m < 4; ++m) { u32x4 w;
; #pragma unroll
;                 for (int q = 0; q < 4; ++q) { const f32x4 v = acc[ai][q >> 1][m][q & 1] * gv[q]; w[q] = pk4_fp8(v[0], v[1], v[2], v[3]); }
;                 *(u32x4*)(MG + (size_t)(pm * 256 + ai * 128 + wr * 64 + m * 16 + fr) * D + col0) = w; }
.LBB0_914:
	s_ashr_i32 s19, s26, 5
	s_mul_hi_i32 s21, s19, 0xc000
	s_mul_i32 s19, s19, 0xc000
	s_add_u32 s28, s36, s19
	v_lshl_or_b32 v2, s64, 8, v190
	s_addc_u32 s29, s37, s21
	v_ashrrev_i32_e32 v3, 31, v2
	v_lshl_add_u64 v[4:5], v[2:3], 2, s[28:29]
	v_add_co_u32_e32 v6, vcc, s62, v4
	s_nop 1
	v_addc_co_u32_e32 v7, vcc, 0, v5, vcc
	global_load_dwordx4 v[6:9], v[6:7], off
	v_lshl_add_u64 v[4:5], v[4:5], 0, s[14:15]
	global_load_dwordx4 v[10:13], v[4:5], off offset:16
	global_load_dwordx4 v[22:25], v[4:5], off offset:32
	global_load_dwordx4 v[26:29], v[4:5], off offset:48
	v_lshl_add_u32 v4, s26, 8, v188
	v_ashrrev_i32_e32 v5, 31, v4
	v_mov_b32_e32 v30, 0
	v_lshlrev_b64 v[14:15], 11, v[4:5]
	v_lshl_add_u64 v[14:15], s[10:11], 0, v[14:15]
	v_lshl_add_u64 v[200:201], v[14:15], 0, v[2:3]
	v_mov_b32_e32 v199, 0
	v_mov_b32_e32 v196, 0
	v_mov_b32_e32 v197, 0
	v_mov_b32_e32 v198, 0
	v_mov_b32_e32 v31, 0
	v_mov_b32_e32 v32, 0
	v_mov_b32_e32 v33, 0
	s_andn2_b64 vcc, exec, s[0:1]
	s_mov_b64 s[0:1], -1
	s_waitcnt vmcnt(0) lgkmcnt(0)
	v_pk_mul_f32 v[16:17], v[10:11], s[16:17] op_sel_hi:[1,0]
	v_pk_mul_f32 v[20:21], v[6:7], s[16:17] op_sel_hi:[1,0]
	v_pk_mul_f32 v[10:11], v[24:25], s[16:17] op_sel_hi:[1,0]
	v_pk_mul_f32 v[24:25], v[158:159], v[20:21]
	v_pk_mul_f32 v[18:19], v[8:9], s[16:17] op_sel_hi:[1,0]
	v_med3_f32 v5, v24, s63, v195
	v_med3_f32 v24, v25, s63, v195
	v_cvt_pk_fp8_f32 v30, v5, v24
	v_pk_mul_f32 v[14:15], v[12:13], s[16:17] op_sel_hi:[1,0]
	v_pk_mul_f32 v[12:13], v[22:23], s[16:17] op_sel_hi:[1,0]
	v_pk_mul_f32 v[22:23], v[160:161], v[18:19]
	v_pk_mul_f32 v[8:9], v[26:27], s[16:17] op_sel_hi:[1,0]
	v_med3_f32 v22, v22, s63, v195
	v_med3_f32 v23, v23, s63, v195
	v_cvt_pk_fp8_f32 v30, v22, v23 op_sel:[0,0,1]
	v_pk_mul_f32 v[22:23], v[126:127], v[8:9]
	v_pk_mul_f32 v[6:7], v[28:29], s[16:17] op_sel_hi:[1,0]
	v_pk_mul_f32 v[28:29], v[154:155], v[16:17]
	v_pk_mul_f32 v[144:145], v[144:145], v[10:11]
	v_pk_mul_f32 v[142:143], v[142:143], v[12:13]
	v_pk_mul_f32 v[150:151], v[150:151], v[20:21]
	v_pk_mul_f32 v[146:147], v[146:147], v[16:17]
	v_pk_mul_f32 v[134:135], v[134:135], v[12:13]
	v_med3_f32 v5, v22, s63, v195
	v_med3_f32 v22, v23, s63, v195
	v_med3_f32 v25, v28, s63, v195
	v_med3_f32 v28, v29, s63, v195
	v_med3_f32 v29, v142, s63, v195
	v_med3_f32 v142, v143, s63, v195
	v_med3_f32 v143, v144, s63, v195
	v_med3_f32 v144, v145, s63, v195
	v_med3_f32 v145, v150, s63, v195
	v_med3_f32 v150, v151, s63, v195
	v_med3_f32 v146, v146, s63, v195
	v_med3_f32 v147, v147, s63, v195
	v_med3_f32 v134, v134, s63, v195
	v_med3_f32 v135, v135, s63, v195
	v_cvt_pk_fp8_f32 v199, v5, v22
	v_cvt_pk_fp8_f32 v196, v145, v150
	v_cvt_pk_fp8_f32 v197, v146, v147
	v_cvt_pk_fp8_f32 v198, v134, v135
	v_pk_mul_f32 v[22:23], v[128:129], v[6:7]
	v_pk_mul_f32 v[152:153], v[152:153], v[18:19]
	v_pk_mul_f32 v[148:149], v[148:149], v[14:15]
	v_pk_mul_f32 v[136:137], v[136:137], v[10:11]
	v_med3_f32 v5, v22, s63, v195
	v_med3_f32 v22, v23, s63, v195
	v_med3_f32 v151, v152, s63, v195
	v_med3_f32 v152, v153, s63, v195
	v_med3_f32 v148, v148, s63, v195
	v_med3_f32 v149, v149, s63, v195
	v_med3_f32 v136, v136, s63, v195
	v_med3_f32 v137, v137, s63, v195
	v_cvt_pk_fp8_f32 v199, v5, v22 op_sel:[0,0,1]
	v_or_b32_e32 v22, 16, v4
	v_cvt_pk_fp8_f32 v196, v151, v152 op_sel:[0,0,1]
	v_cvt_pk_fp8_f32 v197, v148, v149 op_sel:[0,0,1]
	v_cvt_pk_fp8_f32 v198, v136, v137 op_sel:[0,0,1]
	v_ashrrev_i32_e32 v23, 31, v22
	v_lshlrev_b64 v[22:23], 11, v[22:23]
	v_lshl_add_u64 v[22:23], s[10:11], 0, v[22:23]
	v_lshl_add_u64 v[22:23], v[22:23], 0, v[2:3]
	global_store_dwordx4 v[22:23], v[196:199], off
	v_pk_mul_f32 v[22:23], v[130:131], v[20:21]
	v_cvt_pk_fp8_f32 v31, v25, v28
	v_med3_f32 v5, v22, s63, v195
	v_med3_f32 v23, v23, s63, v195
	v_mov_b32_e32 v22, 0
	v_cvt_pk_fp8_f32 v22, v5, v23
	v_pk_mul_f32 v[24:25], v[132:133], v[18:19]
	v_pk_mul_f32 v[26:27], v[156:157], v[14:15]
	v_med3_f32 v5, v24, s63, v195
	v_med3_f32 v23, v25, s63, v195
	v_pk_mul_f32 v[24:25], v[122:123], v[16:17]
	v_cvt_pk_fp8_f32 v22, v5, v23 op_sel:[0,0,1]
	v_med3_f32 v5, v24, s63, v195
	v_med3_f32 v24, v25, s63, v195
	v_mov_b32_e32 v23, 0
	v_cvt_pk_fp8_f32 v23, v5, v24
	v_pk_mul_f32 v[24:25], v[124:125], v[14:15]
	v_med3_f32 v26, v26, s63, v195
	v_med3_f32 v5, v24, s63, v195
	v_med3_f32 v24, v25, s63, v195
	v_cvt_pk_fp8_f32 v23, v5, v24 op_sel:[0,0,1]
	v_pk_mul_f32 v[24:25], v[118:119], v[12:13]
	v_med3_f32 v27, v27, s63, v195
	v_med3_f32 v5, v24, s63, v195
	v_med3_f32 v25, v25, s63, v195
	v_mov_b32_e32 v24, 0
	v_cvt_pk_fp8_f32 v24, v5, v25
	v_cvt_pk_fp8_f32 v31, v26, v27 op_sel:[0,0,1]
	v_pk_mul_f32 v[26:27], v[120:121], v[10:11]
	v_cvt_pk_fp8_f32 v32, v29, v142
	v_med3_f32 v5, v26, s63, v195
	v_med3_f32 v25, v27, s63, v195
	v_pk_mul_f32 v[26:27], v[110:111], v[8:9]
	v_cvt_pk_fp8_f32 v24, v5, v25 op_sel:[0,0,1]
	v_med3_f32 v5, v26, s63, v195
	v_med3_f32 v26, v27, s63, v195
	v_mov_b32_e32 v25, 0
	v_cvt_pk_fp8_f32 v25, v5, v26
	v_pk_mul_f32 v[26:27], v[112:113], v[6:7]
	v_pk_mul_f32 v[28:29], v[88:89], v[10:11]
	v_med3_f32 v5, v26, s63, v195
	v_med3_f32 v26, v27, s63, v195
	v_cvt_pk_fp8_f32 v25, v5, v26 op_sel:[0,0,1]
	v_or_b32_e32 v26, 32, v4
	v_ashrrev_i32_e32 v27, 31, v26
	v_lshlrev_b64 v[26:27], 11, v[26:27]
	v_lshl_add_u64 v[26:27], s[10:11], 0, v[26:27]
	v_lshl_add_u64 v[26:27], v[26:27], 0, v[2:3]
	global_store_dwordx4 v[26:27], v[22:25], off
	v_pk_mul_f32 v[26:27], v[104:105], v[10:11]
	v_pk_mul_f32 v[138:139], v[138:139], v[8:9]
	v_pk_mul_f32 v[22:23], v[114:115], v[20:21]
	v_pk_mul_f32 v[24:25], v[116:117], v[18:19]
	v_med3_f32 v5, v22, s63, v195
	v_med3_f32 v23, v23, s63, v195
	v_mov_b32_e32 v22, 0
; __device__ __forceinline__ unsigned pk4_fp8(float a, float b, float c, float d) { int w = 0; w = __builtin_amdgcn_cvt_pk_fp8_f32(clamp8(a), clamp8(b), w, false); w = __builtin_amdgcn_cvt_pk_fp8_f32(clamp8(c), clamp8(d), w, true); return (unsigned)w; }
;     __device__ __forceinline__ void operator()(AccRef acc, const GUnit& u, int wr, int wc, int fr, int fq) const {
;     ...
;             for (int m = 0; m < 4; ++m) { u32x4 w;
; #pragma unroll
;                 for (int q = 0; q < 4; ++q) { const f32x4 v = acc[ai][q >> 1][m][q & 1] * gv[q]; w[q] = pk4_fp8(v[0], v[1], v[2], v[3]); }
;                 *(u32x4*)(MG + (size_t)(pm * 256 + ai * 128 + wr * 64 + m * 16 + fr) * D + col0) = w; }
	v_cvt_pk_fp8_f32 v22, v5, v23
	v_med3_f32 v5, v24, s63, v195
	v_med3_f32 v23, v25, s63, v195
	v_pk_mul_f32 v[24:25], v[106:107], v[16:17]
	v_cvt_pk_fp8_f32 v22, v5, v23 op_sel:[0,0,1]
	v_med3_f32 v5, v24, s63, v195
	v_med3_f32 v24, v25, s63, v195
	v_mov_b32_e32 v23, 0
	v_cvt_pk_fp8_f32 v23, v5, v24
	v_pk_mul_f32 v[24:25], v[108:109], v[14:15]
	v_med3_f32 v138, v138, s63, v195
	v_med3_f32 v5, v24, s63, v195
	v_med3_f32 v24, v25, s63, v195
	v_cvt_pk_fp8_f32 v23, v5, v24 op_sel:[0,0,1]
	v_pk_mul_f32 v[24:25], v[102:103], v[12:13]
	v_med3_f32 v139, v139, s63, v195
	v_med3_f32 v5, v24, s63, v195
	v_med3_f32 v25, v25, s63, v195
	v_mov_b32_e32 v24, 0
	v_cvt_pk_fp8_f32 v24, v5, v25
	v_med3_f32 v5, v26, s63, v195
	v_med3_f32 v25, v27, s63, v195
	v_pk_mul_f32 v[26:27], v[98:99], v[8:9]
	v_cvt_pk_fp8_f32 v24, v5, v25 op_sel:[0,0,1]
	v_med3_f32 v5, v26, s63, v195
	v_med3_f32 v26, v27, s63, v195
	v_mov_b32_e32 v25, 0
	v_cvt_pk_fp8_f32 v25, v5, v26
	v_pk_mul_f32 v[26:27], v[100:101], v[6:7]
	v_cvt_pk_fp8_f32 v33, v138, v139
	v_med3_f32 v5, v26, s63, v195
	v_med3_f32 v26, v27, s63, v195
	v_cvt_pk_fp8_f32 v25, v5, v26 op_sel:[0,0,1]
	v_or_b32_e32 v26, 48, v4
	v_ashrrev_i32_e32 v27, 31, v26
	v_lshlrev_b64 v[26:27], 11, v[26:27]
	v_lshl_add_u64 v[26:27], s[10:11], 0, v[26:27]
	v_lshl_add_u64 v[26:27], v[26:27], 0, v[2:3]
	global_store_dwordx4 v[26:27], v[22:25], off
	v_add_u32_e32 v26, 0x80, v4
	v_pk_mul_f32 v[140:141], v[140:141], v[6:7]
	v_pk_mul_f32 v[22:23], v[94:95], v[20:21]
	v_pk_mul_f32 v[24:25], v[96:97], v[18:19]
	v_med3_f32 v5, v22, s63, v195
	v_med3_f32 v23, v23, s63, v195
	v_mov_b32_e32 v22, 0
	v_cvt_pk_fp8_f32 v22, v5, v23
	v_med3_f32 v5, v24, s63, v195
	v_med3_f32 v23, v25, s63, v195
	v_pk_mul_f32 v[24:25], v[90:91], v[16:17]
	v_cvt_pk_fp8_f32 v22, v5, v23 op_sel:[0,0,1]
	v_med3_f32 v5, v24, s63, v195
	v_med3_f32 v24, v25, s63, v195
	v_mov_b32_e32 v23, 0
	v_cvt_pk_fp8_f32 v23, v5, v24
	v_pk_mul_f32 v[24:25], v[92:93], v[14:15]
	v_med3_f32 v140, v140, s63, v195
	v_med3_f32 v5, v24, s63, v195
	v_med3_f32 v24, v25, s63, v195
	v_cvt_pk_fp8_f32 v23, v5, v24 op_sel:[0,0,1]
	v_pk_mul_f32 v[24:25], v[86:87], v[12:13]
	v_med3_f32 v141, v141, s63, v195
	v_med3_f32 v5, v24, s63, v195
	v_med3_f32 v25, v25, s63, v195
	v_mov_b32_e32 v24, 0
	v_cvt_pk_fp8_f32 v24, v5, v25
	v_med3_f32 v5, v28, s63, v195
	v_med3_f32 v25, v29, s63, v195
	v_pk_mul_f32 v[28:29], v[78:79], v[8:9]
	v_cvt_pk_fp8_f32 v24, v5, v25 op_sel:[0,0,1]
	v_med3_f32 v5, v28, s63, v195
	v_med3_f32 v27, v29, s63, v195
	v_mov_b32_e32 v25, 0
	v_cvt_pk_fp8_f32 v25, v5, v27
	v_pk_mul_f32 v[28:29], v[80:81], v[6:7]
	v_cvt_pk_fp8_f32 v32, v143, v144 op_sel:[0,0,1]
	v_med3_f32 v5, v28, s63, v195
	v_med3_f32 v27, v29, s63, v195
	v_cvt_pk_fp8_f32 v25, v5, v27 op_sel:[0,0,1]
	v_ashrrev_i32_e32 v27, 31, v26
	v_lshlrev_b64 v[26:27], 11, v[26:27]
	v_lshl_add_u64 v[26:27], s[10:11], 0, v[26:27]
	v_lshl_add_u64 v[26:27], v[26:27], 0, v[2:3]
	global_store_dwordx4 v[26:27], v[22:25], off
	v_pk_mul_f32 v[26:27], v[72:73], v[10:11]
	v_cvt_pk_fp8_f32 v33, v140, v141 op_sel:[0,0,1]
	v_pk_mul_f32 v[22:23], v[82:83], v[20:21]
	v_pk_mul_f32 v[24:25], v[84:85], v[18:19]
	v_med3_f32 v5, v22, s63, v195
	v_med3_f32 v23, v23, s63, v195
	v_mov_b32_e32 v22, 0
	v_cvt_pk_fp8_f32 v22, v5, v23
	v_med3_f32 v5, v24, s63, v195
	v_med3_f32 v23, v25, s63, v195
	v_pk_mul_f32 v[24:25], v[74:75], v[16:17]
	v_cvt_pk_fp8_f32 v22, v5, v23 op_sel:[0,0,1]
	v_med3_f32 v5, v24, s63, v195
	v_med3_f32 v24, v25, s63, v195
	v_mov_b32_e32 v23, 0
	v_cvt_pk_fp8_f32 v23, v5, v24
	v_pk_mul_f32 v[24:25], v[76:77], v[14:15]
	global_store_dwordx4 v[200:201], v[30:33], off
	v_med3_f32 v5, v24, s63, v195
	v_med3_f32 v24, v25, s63, v195
	v_cvt_pk_fp8_f32 v23, v5, v24 op_sel:[0,0,1]
	v_pk_mul_f32 v[24:25], v[70:71], v[12:13]
	s_nop 0
; __device__ __forceinline__ unsigned pk4_fp8(float a, float b, float c, float d) { int w = 0; w = __builtin_amdgcn_cvt_pk_fp8_f32(clamp8(a), clamp8(b), w, false); w = __builtin_amdgcn_cvt_pk_fp8_f32(clamp8(c), clamp8(d), w, true); return (unsigned)w; }
;     __device__ __forceinline__ void operator()(AccRef acc, const GUnit& u, int wr, int wc, int fr, int fq) const {
;     ...
;             for (int m = 0; m < 4; ++m) { u32x4 w;
; #pragma unroll
;                 for (int q = 0; q < 4; ++q) { const f32x4 v = acc[ai][q >> 1][m][q & 1] * gv[q]; w[q] = pk4_fp8(v[0], v[1], v[2], v[3]); }
;                 *(u32x4*)(MG + (size_t)(pm * 256 + ai * 128 + wr * 64 + m * 16 + fr) * D + col0) = w; }
;     }
	v_med3_f32 v5, v24, s63, v195
	v_med3_f32 v25, v25, s63, v195
	v_mov_b32_e32 v24, 0
	v_cvt_pk_fp8_f32 v24, v5, v25
	v_med3_f32 v5, v26, s63, v195
	v_med3_f32 v25, v27, s63, v195
	v_pk_mul_f32 v[26:27], v[62:63], v[8:9]
	v_cvt_pk_fp8_f32 v24, v5, v25 op_sel:[0,0,1]
	v_med3_f32 v5, v26, s63, v195
	v_med3_f32 v26, v27, s63, v195
	v_mov_b32_e32 v25, 0
	v_cvt_pk_fp8_f32 v25, v5, v26
	v_pk_mul_f32 v[26:27], v[64:65], v[6:7]
	s_nop 0
	v_med3_f32 v5, v26, s63, v195
	v_med3_f32 v26, v27, s63, v195
	v_cvt_pk_fp8_f32 v25, v5, v26 op_sel:[0,0,1]
	v_add_u32_e32 v26, 0x90, v4
	v_ashrrev_i32_e32 v27, 31, v26
	v_lshlrev_b64 v[26:27], 11, v[26:27]
	v_lshl_add_u64 v[26:27], s[10:11], 0, v[26:27]
	v_lshl_add_u64 v[26:27], v[26:27], 0, v[2:3]
	global_store_dwordx4 v[26:27], v[22:25], off
	v_pk_mul_f32 v[26:27], v[56:57], v[10:11]
	v_pk_mul_f32 v[10:11], v[40:41], v[10:11]
	v_pk_mul_f32 v[22:23], v[66:67], v[20:21]
	v_pk_mul_f32 v[24:25], v[68:69], v[18:19]
	v_med3_f32 v5, v22, s63, v195
	v_med3_f32 v23, v23, s63, v195
	v_mov_b32_e32 v22, 0
	v_cvt_pk_fp8_f32 v22, v5, v23
	v_med3_f32 v5, v24, s63, v195
	v_med3_f32 v23, v25, s63, v195
	v_pk_mul_f32 v[24:25], v[58:59], v[16:17]
	v_cvt_pk_fp8_f32 v22, v5, v23 op_sel:[0,0,1]
	v_med3_f32 v5, v24, s63, v195
	v_med3_f32 v24, v25, s63, v195
	v_mov_b32_e32 v23, 0
	v_cvt_pk_fp8_f32 v23, v5, v24
	v_pk_mul_f32 v[24:25], v[60:61], v[14:15]
	v_pk_mul_f32 v[20:21], v[50:51], v[20:21]
	v_med3_f32 v5, v24, s63, v195
	v_med3_f32 v24, v25, s63, v195
	v_cvt_pk_fp8_f32 v23, v5, v24 op_sel:[0,0,1]
	v_pk_mul_f32 v[24:25], v[54:55], v[12:13]
	v_med3_f32 v21, v21, s63, v195
	v_med3_f32 v5, v24, s63, v195
	v_med3_f32 v25, v25, s63, v195
	v_mov_b32_e32 v24, 0
	v_cvt_pk_fp8_f32 v24, v5, v25
	v_med3_f32 v5, v26, s63, v195
	v_med3_f32 v25, v27, s63, v195
	v_pk_mul_f32 v[26:27], v[46:47], v[8:9]
	v_cvt_pk_fp8_f32 v24, v5, v25 op_sel:[0,0,1]
	v_med3_f32 v5, v26, s63, v195
	v_med3_f32 v26, v27, s63, v195
	v_mov_b32_e32 v25, 0
	v_cvt_pk_fp8_f32 v25, v5, v26
	v_pk_mul_f32 v[26:27], v[48:49], v[6:7]
	v_pk_mul_f32 v[18:19], v[52:53], v[18:19]
	v_med3_f32 v5, v26, s63, v195
	v_med3_f32 v26, v27, s63, v195
	v_cvt_pk_fp8_f32 v25, v5, v26 op_sel:[0,0,1]
	v_med3_f32 v5, v20, s63, v195
	v_mov_b32_e32 v20, 0
	v_cvt_pk_fp8_f32 v20, v5, v21
	v_med3_f32 v5, v18, s63, v195
	v_med3_f32 v18, v19, s63, v195
	v_pk_mul_f32 v[16:17], v[42:43], v[16:17]
	v_add_u32_e32 v26, 0xa0, v4
	v_cvt_pk_fp8_f32 v20, v5, v18 op_sel:[0,0,1]
	v_med3_f32 v5, v16, s63, v195
	v_med3_f32 v16, v17, s63, v195
	v_mov_b32_e32 v21, 0
	v_ashrrev_i32_e32 v27, 31, v26
	v_cvt_pk_fp8_f32 v21, v5, v16
	v_lshlrev_b64 v[26:27], 11, v[26:27]
	v_lshl_add_u64 v[26:27], s[10:11], 0, v[26:27]
	v_pk_mul_f32 v[14:15], v[44:45], v[14:15]
	v_lshl_add_u64 v[26:27], v[26:27], 0, v[2:3]
	v_med3_f32 v5, v14, s63, v195
	v_med3_f32 v14, v15, s63, v195
	v_pk_mul_f32 v[12:13], v[38:39], v[12:13]
	global_store_dwordx4 v[26:27], v[22:25], off
	v_cvt_pk_fp8_f32 v21, v5, v14 op_sel:[0,0,1]
	v_med3_f32 v5, v12, s63, v195
	v_med3_f32 v12, v13, s63, v195
	v_mov_b32_e32 v22, 0
	v_cvt_pk_fp8_f32 v22, v5, v12
	v_med3_f32 v5, v10, s63, v195
	v_med3_f32 v10, v11, s63, v195
	v_pk_mul_f32 v[8:9], v[34:35], v[8:9]
	v_cvt_pk_fp8_f32 v22, v5, v10 op_sel:[0,0,1]
	v_med3_f32 v5, v8, s63, v195
	v_med3_f32 v8, v9, s63, v195
	v_mov_b32_e32 v23, 0
	v_cvt_pk_fp8_f32 v23, v5, v8
	v_pk_mul_f32 v[6:7], v[36:37], v[6:7]
	v_add_u32_e32 v4, 0xb0, v4
	v_med3_f32 v5, v6, s63, v195
	v_med3_f32 v6, v7, s63, v195
	v_cvt_pk_fp8_f32 v23, v5, v6 op_sel:[0,0,1]
	v_ashrrev_i32_e32 v5, 31, v4
	v_lshlrev_b64 v[4:5], 11, v[4:5]
	v_lshl_add_u64 v[4:5], s[10:11], 0, v[4:5]
	v_lshl_add_u64 v[2:3], v[4:5], 0, v[2:3]
	global_store_dwordx4 v[2:3], v[20:23], off
	s_cbranch_vccnz .LBB0_903
	s_andn2_b64 vcc, exec, s[8:9]
	s_cbranch_vccnz .LBB0_902
	s_branch .LBB0_902

; __device__ __forceinline__ unsigned pk4_fp8(float a, float b, float c, float d) { int w = 0; w = __builtin_amdgcn_cvt_pk_fp8_f32(clamp8(a), clamp8(b), w, false); w = __builtin_amdgcn_cvt_pk_fp8_f32(clamp8(c), clamp8(d), w, true); return (unsigned)w; }
;     __device__ __forceinline__ void operator()(AccRef acc, const GUnit& u, int wr, int wc, int fr, int fq) const {
;         const int e = u.x0, rt = u.x1, ct = u.x2, cnt = u.x3; const int* rl = rowlist + (size_t)e * ECAP; const int p0 = rt * 256 + wr * 64 + fr;
;         unsigned ent[2][4];
; #pragma unroll
;         for (int ai = 0; ai < 2; ++ai)
; #pragma unroll
;             for (int m = 0; m < 4; ++m) { int p = p0 + ai * 128 + m * 16; p = p < cnt ? p : cnt - 1; ent[ai][m] = (unsigned)rl[p]; }
; #pragma unroll
;         for (int ai = 0; ai < 2; ++ai)
; #pragma unroll
;             for (int m = 0; m < 4; ++m) { const int p = p0 + ai * 128 + m * 16;
;                 if (p < cnt) { u32x4 w;
; #pragma unroll
;                     for (int q = 0; q < 4; ++q) { const f32x4 v = acc[ai][q >> 1][m][q & 1] * (W8_INV * Y8_SCALE); w[q] = pk4_fp8(v[0], v[1], v[2], v[3]); }
;                     *(u32x4*)(Y + (size_t)ent[ai][m] * D + ct * 256 + wc * 64 + 16 * fq) = w; } }
.LBB0_1141:
	s_ashr_i32 s23, s22, 31
	s_lshl_b64 s[22:23], s[22:23], 17
	s_add_u32 s26, s49, s22
	v_lshl_add_u32 v16, s66, 8, v186
	s_addc_u32 s27, s50, s23
	s_add_i32 s22, s48, -1
	v_or_b32_e32 v15, 16, v16
	v_min_i32_e32 v2, s22, v15
	v_ashrrev_i32_e32 v3, 31, v2
	v_or_b32_e32 v13, 32, v16
	v_lshl_add_u64 v[18:19], v[2:3], 2, s[26:27]
	v_min_i32_e32 v2, s22, v13
	v_ashrrev_i32_e32 v3, 31, v2
	v_or_b32_e32 v11, 48, v16
	v_lshl_add_u64 v[20:21], v[2:3], 2, s[26:27]
	v_min_i32_e32 v2, s22, v11
	v_ashrrev_i32_e32 v3, 31, v2
	v_add_u32_e32 v9, 0x80, v16
	v_lshl_add_u64 v[22:23], v[2:3], 2, s[26:27]
	v_min_i32_e32 v2, s22, v9
	v_ashrrev_i32_e32 v3, 31, v2
	v_add_u32_e32 v7, 0x90, v16
	v_lshl_add_u64 v[24:25], v[2:3], 2, s[26:27]
	v_min_i32_e32 v2, s22, v7
	v_ashrrev_i32_e32 v3, 31, v2
	v_add_u32_e32 v5, 0xa0, v16
	v_lshl_add_u64 v[26:27], v[2:3], 2, s[26:27]
	v_min_i32_e32 v2, s22, v5
	v_ashrrev_i32_e32 v3, 31, v2
	v_lshl_add_u64 v[28:29], v[2:3], 2, s[26:27]
	v_add_u32_e32 v3, 0xb0, v16
	v_min_i32_e32 v30, s22, v3
	v_ashrrev_i32_e32 v31, 31, v30
	v_lshl_add_u64 v[30:31], v[30:31], 2, s[26:27]
	global_load_dword v14, v[18:19], off
	global_load_dword v12, v[20:21], off
	global_load_dword v10, v[22:23], off
	global_load_dword v8, v[24:25], off
	global_load_dword v6, v[26:27], off
	global_load_dword v4, v[28:29], off
	global_load_dword v2, v[30:31], off
	s_lshl_b32 s22, s65, 8
	s_ashr_i32 s23, s22, 31
	v_cmp_gt_i32_e32 vcc, s48, v16
	s_and_saveexec_b64 s[24:25], vcc
	s_cbranch_execz .LBB0_1150
	v_ashrrev_i32_e32 v17, 31, v16
	v_lshl_add_u64 v[16:17], v[16:17], 2, s[26:27]
	global_load_dword v176, v[16:17], off
	v_pk_mul_f32 v[16:17], v[158:159], s[14:15] op_sel_hi:[1,0]
	s_nop 0
	v_med3_f32 v18, v16, s59, v193
	v_med3_f32 v17, v17, s59, v193
	v_mov_b32_e32 v16, v177
	v_cvt_pk_fp8_f32 v16, v18, v17
	v_pk_mul_f32 v[18:19], v[160:161], s[14:15] op_sel_hi:[1,0]
	s_nop 0
	v_med3_f32 v17, v18, s59, v193
	v_med3_f32 v18, v19, s59, v193
	v_cvt_pk_fp8_f32 v16, v17, v18 op_sel:[0,0,1]
	v_pk_mul_f32 v[18:19], v[154:155], s[14:15] op_sel_hi:[1,0]
	v_mov_b32_e32 v17, v177
	v_med3_f32 v18, v18, s59, v193
	v_med3_f32 v19, v19, s59, v193
	v_cvt_pk_fp8_f32 v17, v18, v19
	v_pk_mul_f32 v[18:19], v[156:157], s[14:15] op_sel_hi:[1,0]
	s_nop 0
	v_med3_f32 v18, v18, s59, v193
	v_med3_f32 v19, v19, s59, v193
	v_cvt_pk_fp8_f32 v17, v18, v19 op_sel:[0,0,1]
	v_pk_mul_f32 v[18:19], v[150:151], s[14:15] op_sel_hi:[1,0]
	s_nop 0
	v_med3_f32 v20, v18, s59, v193
	v_med3_f32 v19, v19, s59, v193
	v_mov_b32_e32 v18, v177
	v_cvt_pk_fp8_f32 v18, v20, v19
	v_pk_mul_f32 v[20:21], v[152:153], s[14:15] op_sel_hi:[1,0]
	s_nop 0
	v_med3_f32 v19, v20, s59, v193
	v_med3_f32 v20, v21, s59, v193
	v_cvt_pk_fp8_f32 v18, v19, v20 op_sel:[0,0,1]
	v_pk_mul_f32 v[20:21], v[146:147], s[14:15] op_sel_hi:[1,0]
	v_mov_b32_e32 v19, v177
	v_med3_f32 v20, v20, s59, v193
	v_med3_f32 v21, v21, s59, v193
	v_cvt_pk_fp8_f32 v19, v20, v21
	v_pk_mul_f32 v[20:21], v[148:149], s[14:15] op_sel_hi:[1,0]
	s_nop 0
	v_med3_f32 v20, v20, s59, v193
	v_med3_f32 v21, v21, s59, v193
	v_cvt_pk_fp8_f32 v19, v20, v21 op_sel:[0,0,1]
	s_waitcnt vmcnt(0) lgkmcnt(0)
	v_lshlrev_b64 v[20:21], 11, v[176:177]
	v_lshl_add_u64 v[20:21], s[10:11], 0, v[20:21]
	v_lshl_add_u64 v[20:21], v[20:21], 0, s[22:23]
	v_lshl_add_u64 v[20:21], v[20:21], 0, s[6:7]
	v_lshl_add_u64 v[20:21], v[20:21], 0, v[162:163]
	global_store_dwordx4 v[20:21], v[16:19], off
	s_or_b64 exec, exec, s[24:25]
	v_cmp_gt_i32_e32 vcc, s48, v15
	s_and_saveexec_b64 s[24:25], vcc
	s_cbranch_execnz .LBB0_1151
